# v67 plus vt_transpose requesting all of a workgroup's tile loads up front
# speedup vs baseline: 1.0051x; 1.0006x over previous
; #define LAS __attribute__((address_space(3)))
; __device__ __forceinline__ void vt_transpose(const Ctx& c, const bf16_t* proj, bf16_t* vt) {
;     ...
;     for (int it = c.bid; it < 3 * 2 * 256; it += c.G) {
;         const int which = it / 512, g = (it >> 8) & 1, tt = it & 255;
;         const int col = (which == 0 ? PC_VS : (which == 1 ? PC_VW : PC_SV)) + g * 64;
;         { const int tok = c.tid >> 3, ch = c.tid & 7; const u32x4 w = *(const u32x4*)(proj + (size_t)(tt * 64 + tok) * PLD + col + ch * 8);
;           *(LAS u32x4*)(tl + tok * 72 + ch * 8) = w; }
.LBB0_500:
	s_or_b64 exec, exec, s[4:5]
	s_cmpk_gt_i32 s14, 0x61f
	s_cbranch_scc1 .LBB0_503
	v_ashrrev_i32_e32 v2, 3, v151
	v_mul_lo_u32 v3, v2, s67
	v_lshlrev_b32_e32 v0, 3, v151
	v_add_u32_e32 v4, 0, v3
	s_movk_i32 s0, 0xff72
	v_and_b32_e32 v0, 56, v0
	v_mad_u64_u32 v[8:9], s[0:1], v2, s0, v[4:5]
	v_ashrrev_i32_e32 v3, 31, v2
	v_lshl_add_u32 v6, v0, 1, v4
	v_mul_u32_u24_e32 v7, 0x90, v0
	v_lshlrev_b64 v[4:5], 15, v[2:3]
	s_lshl_b32 s0, s14, 6
	v_lshl_add_u64 v[4:5], s[82:83], 0, v[4:5]
	s_addk_i32 s0, 0xf800
	v_lshlrev_b32_e32 v0, 1, v0
	v_add_u32_e32 v3, v8, v7
	v_readlane_b32 s5, v252, 52
	s_mov_b32 s6, 0x5040100
	s_mov_b32 s7, s10
	s_min_i32 s15, s10, 0x5ff
	s_bfe_u32 s1, s15, 0x10008
	s_add_i32 s2, s15, 0x1ff
	s_and_b32 s3, s15, 0xfffffe00
	s_cmpk_eq_i32 s3, 0x200
	s_movk_i32 s3, 0xb80
	s_cselect_b32 s3, s3, 0xf80
	s_cmpk_gt_u32 s2, 0x3fe
	s_cselect_b32 s2, s3, 0xa80
	s_lshl_b32 s4, s15, 6
	s_and_b32 s4, s4, 0x3fc0
	v_add_u32_e32 v112, s4, v2
	v_ashrrev_i32_e32 v113, 31, v112
	v_lshlrev_b64 v[112:113], 13, v[112:113]
	s_lshl_b32 s2, s2, 1
	s_lshl_b32 s3, s1, 7
	v_lshl_add_u64 v[112:113], s[80:81], 0, v[112:113]
	s_or_b32 s42, s3, s2
	v_lshl_add_u64 v[112:113], v[112:113], 0, s[42:43]
	v_lshl_add_u64 v[112:113], v[112:113], 0, v[0:1]
	global_load_dwordx4 v[84:87], v[112:113], off
	s_add_i32 s10, s10, s11
	s_min_i32 s15, s10, 0x5ff
	s_bfe_u32 s1, s15, 0x10008
	s_add_i32 s2, s15, 0x1ff
	s_and_b32 s3, s15, 0xfffffe00
	s_cmpk_eq_i32 s3, 0x200
	s_movk_i32 s3, 0xb80
	s_cselect_b32 s3, s3, 0xf80
	s_cmpk_gt_u32 s2, 0x3fe
	s_cselect_b32 s2, s3, 0xa80
	s_lshl_b32 s4, s15, 6
	s_and_b32 s4, s4, 0x3fc0
	v_add_u32_e32 v114, s4, v2
	v_ashrrev_i32_e32 v115, 31, v114
	v_lshlrev_b64 v[114:115], 13, v[114:115]
	s_lshl_b32 s2, s2, 1
	s_lshl_b32 s3, s1, 7
	v_lshl_add_u64 v[114:115], s[80:81], 0, v[114:115]
	s_or_b32 s42, s3, s2
	v_lshl_add_u64 v[114:115], v[114:115], 0, s[42:43]
	v_lshl_add_u64 v[114:115], v[114:115], 0, v[0:1]
	global_load_dwordx4 v[88:91], v[114:115], off
	s_add_i32 s10, s10, s11
	s_min_i32 s15, s10, 0x5ff
	s_bfe_u32 s1, s15, 0x10008
	s_add_i32 s2, s15, 0x1ff
	s_and_b32 s3, s15, 0xfffffe00
	s_cmpk_eq_i32 s3, 0x200
	s_movk_i32 s3, 0xb80
	s_cselect_b32 s3, s3, 0xf80
	s_cmpk_gt_u32 s2, 0x3fe
	s_cselect_b32 s2, s3, 0xa80
	s_lshl_b32 s4, s15, 6
	s_and_b32 s4, s4, 0x3fc0
	v_add_u32_e32 v112, s4, v2
	v_ashrrev_i32_e32 v113, 31, v112
	v_lshlrev_b64 v[112:113], 13, v[112:113]
	s_lshl_b32 s2, s2, 1
	s_lshl_b32 s3, s1, 7
	v_lshl_add_u64 v[112:113], s[80:81], 0, v[112:113]
	s_or_b32 s42, s3, s2
	v_lshl_add_u64 v[112:113], v[112:113], 0, s[42:43]
	v_lshl_add_u64 v[112:113], v[112:113], 0, v[0:1]
	global_load_dwordx4 v[92:95], v[112:113], off
	s_add_i32 s10, s10, s11
	s_min_i32 s15, s10, 0x5ff
	s_bfe_u32 s1, s15, 0x10008
	s_add_i32 s2, s15, 0x1ff
	s_and_b32 s3, s15, 0xfffffe00
	s_cmpk_eq_i32 s3, 0x200
	s_movk_i32 s3, 0xb80
	s_cselect_b32 s3, s3, 0xf80
	s_cmpk_gt_u32 s2, 0x3fe
	s_cselect_b32 s2, s3, 0xa80
	s_lshl_b32 s4, s15, 6
	s_and_b32 s4, s4, 0x3fc0
	v_add_u32_e32 v114, s4, v2
	v_ashrrev_i32_e32 v115, 31, v114
	v_lshlrev_b64 v[114:115], 13, v[114:115]
	s_lshl_b32 s2, s2, 1
	s_lshl_b32 s3, s1, 7
	v_lshl_add_u64 v[114:115], s[80:81], 0, v[114:115]
	s_or_b32 s42, s3, s2
	v_lshl_add_u64 v[114:115], v[114:115], 0, s[42:43]
	v_lshl_add_u64 v[114:115], v[114:115], 0, v[0:1]
	global_load_dwordx4 v[96:99], v[114:115], off
	s_add_i32 s10, s10, s11
	s_min_i32 s15, s10, 0x5ff
	s_bfe_u32 s1, s15, 0x10008
	s_add_i32 s2, s15, 0x1ff
	s_and_b32 s3, s15, 0xfffffe00
	s_cmpk_eq_i32 s3, 0x200
	s_movk_i32 s3, 0xb80
	s_cselect_b32 s3, s3, 0xf80
	s_cmpk_gt_u32 s2, 0x3fe
	s_cselect_b32 s2, s3, 0xa80
	s_lshl_b32 s4, s15, 6
	s_and_b32 s4, s4, 0x3fc0
	v_add_u32_e32 v112, s4, v2
	v_ashrrev_i32_e32 v113, 31, v112
	v_lshlrev_b64 v[112:113], 13, v[112:113]
	s_lshl_b32 s2, s2, 1
	s_lshl_b32 s3, s1, 7
	v_lshl_add_u64 v[112:113], s[80:81], 0, v[112:113]
	s_or_b32 s42, s3, s2
	v_lshl_add_u64 v[112:113], v[112:113], 0, s[42:43]
	v_lshl_add_u64 v[112:113], v[112:113], 0, v[0:1]
	global_load_dwordx4 v[100:103], v[112:113], off
	s_add_i32 s10, s10, s11
	s_min_i32 s15, s10, 0x5ff
	s_bfe_u32 s1, s15, 0x10008
	s_add_i32 s2, s15, 0x1ff
	s_and_b32 s3, s15, 0xfffffe00
	s_cmpk_eq_i32 s3, 0x200
	s_movk_i32 s3, 0xb80
	s_cselect_b32 s3, s3, 0xf80
	s_cmpk_gt_u32 s2, 0x3fe
	s_cselect_b32 s2, s3, 0xa80
	s_lshl_b32 s4, s15, 6
	s_and_b32 s4, s4, 0x3fc0
	v_add_u32_e32 v114, s4, v2
	v_ashrrev_i32_e32 v115, 31, v114
	v_lshlrev_b64 v[114:115], 13, v[114:115]
	s_lshl_b32 s2, s2, 1
	s_lshl_b32 s3, s1, 7
	v_lshl_add_u64 v[114:115], s[80:81], 0, v[114:115]
	s_or_b32 s42, s3, s2
	v_lshl_add_u64 v[114:115], v[114:115], 0, s[42:43]
	v_lshl_add_u64 v[114:115], v[114:115], 0, v[0:1]
	global_load_dwordx4 v[104:107], v[114:115], off
	s_add_i32 s10, s10, s11
	s_min_i32 s15, s10, 0x5ff
	s_bfe_u32 s1, s15, 0x10008
	s_add_i32 s2, s15, 0x1ff
	s_and_b32 s3, s15, 0xfffffe00
	s_cmpk_eq_i32 s3, 0x200
	s_movk_i32 s3, 0xb80
	s_cselect_b32 s3, s3, 0xf80
	s_cmpk_gt_u32 s2, 0x3fe
	s_cselect_b32 s2, s3, 0xa80
	s_lshl_b32 s4, s15, 6
	s_and_b32 s4, s4, 0x3fc0
	v_add_u32_e32 v112, s4, v2
	v_ashrrev_i32_e32 v113, 31, v112
	v_lshlrev_b64 v[112:113], 13, v[112:113]
	s_lshl_b32 s2, s2, 1
	s_lshl_b32 s3, s1, 7
	v_lshl_add_u64 v[112:113], s[80:81], 0, v[112:113]
	s_or_b32 s42, s3, s2
	v_lshl_add_u64 v[112:113], v[112:113], 0, s[42:43]
	v_lshl_add_u64 v[112:113], v[112:113], 0, v[0:1]
	global_load_dwordx4 v[108:111], v[112:113], off
	s_add_i32 s10, s10, s11
	s_mov_b32 s10, s7
	s_cmpk_lt_i32 s10, 0x600
	s_cbranch_scc0 .LBB0_503
; #define LAS __attribute__((address_space(3)))
; __device__ __forceinline__ void vt_transpose(const Ctx& c, const bf16_t* proj, bf16_t* vt) {
;     ...
;     for (int it = c.bid; it < 3 * 2 * 256; it += c.G) {
;         const int which = it / 512, g = (it >> 8) & 1, tt = it & 255;
;         const int col = (which == 0 ? PC_VS : (which == 1 ? PC_VW : PC_SV)) + g * 64;
;         { const int tok = c.tid >> 3, ch = c.tid & 7; const u32x4 w = *(const u32x4*)(proj + (size_t)(tt * 64 + tok) * PLD + col + ch * 8);
;           *(LAS u32x4*)(tl + tok * 72 + ch * 8) = w; }
;         __syncthreads();
;         { const int d = c.tid >> 3, ch = c.tid & 7; unsigned short e[8];
; #pragma unroll
;           for (int k = 0; k < 8; ++k) e[k] = tl[(ch * 8 + k) * 72 + d];
;           u32x4 w; w.x = e[0] | ((unsigned)e[1] << 16); w.y = e[2] | ((unsigned)e[3] << 16); w.z = e[4] | ((unsigned)e[5] << 16); w.w = e[6] | ((unsigned)e[7] << 16);
;           *(u32x4*)(vt + ((size_t)(which * 2 + g) * 64 + d) * T + tt * 64 + ch * 8) = w; }
;         __syncthreads();
;     }
	s_bfe_u32 s1, s10, 0x10008
	s_lshl_b32 s4, s10, 6
	s_and_b32 s4, s4, 0x3fc0
	s_ashr_i32 s2, s10, 31
	s_lshr_b32 s2, s2, 23
	s_add_i32 s2, s10, s2
	s_ashr_i32 s2, s2, 9
	s_lshl_b32 s2, s2, 1
	s_or_b32 s2, s2, s1
	s_ashr_i32 s3, s2, 31
	s_lshl_b64 s[2:3], s[2:3], 21
	s_lshl_b32 s42, s4, 1
	s_add_i32 s10, s10, s11
	s_waitcnt vmcnt(6)
	ds_write_b128 v6, v[84:87]
	s_waitcnt lgkmcnt(0)
	s_barrier
	ds_read_u16 v7, v3
	ds_read_u16 v8, v3 offset:144
	ds_read_u16 v9, v3 offset:288
	ds_read_u16 v12, v3 offset:432
	ds_read_u16 v10, v3 offset:576
	ds_read_u16 v13, v3 offset:720
	ds_read_u16 v11, v3 offset:864
	ds_read_u16 v14, v3 offset:1008
	s_waitcnt lgkmcnt(4)
	v_perm_b32 v9, v12, v9, s6
	v_perm_b32 v8, v8, v7, s6
	s_waitcnt lgkmcnt(2)
	v_perm_b32 v10, v13, v10, s6
	v_lshl_add_u64 v[12:13], v[4:5], 0, s[2:3]
	v_lshl_add_u64 v[12:13], v[12:13], 0, s[42:43]
	s_waitcnt lgkmcnt(0)
	v_perm_b32 v11, v14, v11, s6
	v_lshl_add_u64 v[12:13], v[12:13], 0, v[0:1]
	global_store_dwordx4 v[12:13], v[8:11], off
	s_barrier
	s_cmpk_lt_i32 s10, 0x600
	s_cbranch_scc0 .LBB0_503
	s_bfe_u32 s1, s10, 0x10008
	s_lshl_b32 s4, s10, 6
	s_and_b32 s4, s4, 0x3fc0
	s_ashr_i32 s2, s10, 31
	s_lshr_b32 s2, s2, 23
	s_add_i32 s2, s10, s2
	s_ashr_i32 s2, s2, 9
	s_lshl_b32 s2, s2, 1
	s_or_b32 s2, s2, s1
	s_ashr_i32 s3, s2, 31
	s_lshl_b64 s[2:3], s[2:3], 21
	s_lshl_b32 s42, s4, 1
	s_add_i32 s10, s10, s11
	s_waitcnt vmcnt(5)
	ds_write_b128 v6, v[88:91]
	s_waitcnt lgkmcnt(0)
	s_barrier
	ds_read_u16 v7, v3
	ds_read_u16 v8, v3 offset:144
	ds_read_u16 v9, v3 offset:288
	ds_read_u16 v12, v3 offset:432
	ds_read_u16 v10, v3 offset:576
	ds_read_u16 v13, v3 offset:720
	ds_read_u16 v11, v3 offset:864
	ds_read_u16 v14, v3 offset:1008
	s_waitcnt lgkmcnt(4)
	v_perm_b32 v9, v12, v9, s6
	v_perm_b32 v8, v8, v7, s6
	s_waitcnt lgkmcnt(2)
	v_perm_b32 v10, v13, v10, s6
	v_lshl_add_u64 v[12:13], v[4:5], 0, s[2:3]
	v_lshl_add_u64 v[12:13], v[12:13], 0, s[42:43]
	s_waitcnt lgkmcnt(0)
	v_perm_b32 v11, v14, v11, s6
	v_lshl_add_u64 v[12:13], v[12:13], 0, v[0:1]
	global_store_dwordx4 v[12:13], v[8:11], off
	s_barrier
	s_cmpk_lt_i32 s10, 0x600
	s_cbranch_scc0 .LBB0_503
	s_bfe_u32 s1, s10, 0x10008
	s_lshl_b32 s4, s10, 6
	s_and_b32 s4, s4, 0x3fc0
	s_ashr_i32 s2, s10, 31
	s_lshr_b32 s2, s2, 23
	s_add_i32 s2, s10, s2
	s_ashr_i32 s2, s2, 9
	s_lshl_b32 s2, s2, 1
	s_or_b32 s2, s2, s1
	s_ashr_i32 s3, s2, 31
	s_lshl_b64 s[2:3], s[2:3], 21
	s_lshl_b32 s42, s4, 1
	s_add_i32 s10, s10, s11
	s_waitcnt vmcnt(4)
	ds_write_b128 v6, v[92:95]
	s_waitcnt lgkmcnt(0)
	s_barrier
	ds_read_u16 v7, v3
	ds_read_u16 v8, v3 offset:144
	ds_read_u16 v9, v3 offset:288
	ds_read_u16 v12, v3 offset:432
	ds_read_u16 v10, v3 offset:576
	ds_read_u16 v13, v3 offset:720
	ds_read_u16 v11, v3 offset:864
	ds_read_u16 v14, v3 offset:1008
	s_waitcnt lgkmcnt(4)
	v_perm_b32 v9, v12, v9, s6
	v_perm_b32 v8, v8, v7, s6
	s_waitcnt lgkmcnt(2)
	v_perm_b32 v10, v13, v10, s6
	v_lshl_add_u64 v[12:13], v[4:5], 0, s[2:3]
	v_lshl_add_u64 v[12:13], v[12:13], 0, s[42:43]
	s_waitcnt lgkmcnt(0)
	v_perm_b32 v11, v14, v11, s6
	v_lshl_add_u64 v[12:13], v[12:13], 0, v[0:1]
	global_store_dwordx4 v[12:13], v[8:11], off
	s_barrier
	s_cmpk_lt_i32 s10, 0x600
	s_cbranch_scc0 .LBB0_503
	s_bfe_u32 s1, s10, 0x10008
	s_lshl_b32 s4, s10, 6
	s_and_b32 s4, s4, 0x3fc0
	s_ashr_i32 s2, s10, 31
	s_lshr_b32 s2, s2, 23
	s_add_i32 s2, s10, s2
	s_ashr_i32 s2, s2, 9
	s_lshl_b32 s2, s2, 1
	s_or_b32 s2, s2, s1
	s_ashr_i32 s3, s2, 31
	s_lshl_b64 s[2:3], s[2:3], 21
	s_lshl_b32 s42, s4, 1
	s_add_i32 s10, s10, s11
	s_waitcnt vmcnt(3)
	ds_write_b128 v6, v[96:99]
	s_waitcnt lgkmcnt(0)
	s_barrier
; #define LAS __attribute__((address_space(3)))
; __device__ __forceinline__ void vt_transpose(const Ctx& c, const bf16_t* proj, bf16_t* vt) {
;     ...
;     for (int it = c.bid; it < 3 * 2 * 256; it += c.G) {
;         const int which = it / 512, g = (it >> 8) & 1, tt = it & 255;
;         const int col = (which == 0 ? PC_VS : (which == 1 ? PC_VW : PC_SV)) + g * 64;
;         { const int tok = c.tid >> 3, ch = c.tid & 7; const u32x4 w = *(const u32x4*)(proj + (size_t)(tt * 64 + tok) * PLD + col + ch * 8);
;           *(LAS u32x4*)(tl + tok * 72 + ch * 8) = w; }
;         __syncthreads();
;         { const int d = c.tid >> 3, ch = c.tid & 7; unsigned short e[8];
; #pragma unroll
;           for (int k = 0; k < 8; ++k) e[k] = tl[(ch * 8 + k) * 72 + d];
;           u32x4 w; w.x = e[0] | ((unsigned)e[1] << 16); w.y = e[2] | ((unsigned)e[3] << 16); w.z = e[4] | ((unsigned)e[5] << 16); w.w = e[6] | ((unsigned)e[7] << 16);
;           *(u32x4*)(vt + ((size_t)(which * 2 + g) * 64 + d) * T + tt * 64 + ch * 8) = w; }
;         __syncthreads();
;     }
	ds_read_u16 v7, v3
	ds_read_u16 v8, v3 offset:144
	ds_read_u16 v9, v3 offset:288
	ds_read_u16 v12, v3 offset:432
	ds_read_u16 v10, v3 offset:576
	ds_read_u16 v13, v3 offset:720
	ds_read_u16 v11, v3 offset:864
	ds_read_u16 v14, v3 offset:1008
	s_waitcnt lgkmcnt(4)
	v_perm_b32 v9, v12, v9, s6
	v_perm_b32 v8, v8, v7, s6
	s_waitcnt lgkmcnt(2)
	v_perm_b32 v10, v13, v10, s6
	v_lshl_add_u64 v[12:13], v[4:5], 0, s[2:3]
	v_lshl_add_u64 v[12:13], v[12:13], 0, s[42:43]
	s_waitcnt lgkmcnt(0)
	v_perm_b32 v11, v14, v11, s6
	v_lshl_add_u64 v[12:13], v[12:13], 0, v[0:1]
	global_store_dwordx4 v[12:13], v[8:11], off
	s_barrier
	s_cmpk_lt_i32 s10, 0x600
	s_cbranch_scc0 .LBB0_503
	s_bfe_u32 s1, s10, 0x10008
	s_lshl_b32 s4, s10, 6
	s_and_b32 s4, s4, 0x3fc0
	s_ashr_i32 s2, s10, 31
	s_lshr_b32 s2, s2, 23
	s_add_i32 s2, s10, s2
	s_ashr_i32 s2, s2, 9
	s_lshl_b32 s2, s2, 1
	s_or_b32 s2, s2, s1
	s_ashr_i32 s3, s2, 31
	s_lshl_b64 s[2:3], s[2:3], 21
	s_lshl_b32 s42, s4, 1
	s_add_i32 s10, s10, s11
	s_waitcnt vmcnt(2)
	ds_write_b128 v6, v[100:103]
	s_waitcnt lgkmcnt(0)
	s_barrier
	ds_read_u16 v7, v3
	ds_read_u16 v8, v3 offset:144
	ds_read_u16 v9, v3 offset:288
	ds_read_u16 v12, v3 offset:432
	ds_read_u16 v10, v3 offset:576
	ds_read_u16 v13, v3 offset:720
	ds_read_u16 v11, v3 offset:864
	ds_read_u16 v14, v3 offset:1008
	s_waitcnt lgkmcnt(4)
	v_perm_b32 v9, v12, v9, s6
	v_perm_b32 v8, v8, v7, s6
	s_waitcnt lgkmcnt(2)
	v_perm_b32 v10, v13, v10, s6
	v_lshl_add_u64 v[12:13], v[4:5], 0, s[2:3]
	v_lshl_add_u64 v[12:13], v[12:13], 0, s[42:43]
	s_waitcnt lgkmcnt(0)
	v_perm_b32 v11, v14, v11, s6
	v_lshl_add_u64 v[12:13], v[12:13], 0, v[0:1]
	global_store_dwordx4 v[12:13], v[8:11], off
	s_barrier
	s_cmpk_lt_i32 s10, 0x600
	s_cbranch_scc0 .LBB0_503
	s_bfe_u32 s1, s10, 0x10008
	s_lshl_b32 s4, s10, 6
	s_and_b32 s4, s4, 0x3fc0
	s_ashr_i32 s2, s10, 31
	s_lshr_b32 s2, s2, 23
	s_add_i32 s2, s10, s2
	s_ashr_i32 s2, s2, 9
	s_lshl_b32 s2, s2, 1
	s_or_b32 s2, s2, s1
	s_ashr_i32 s3, s2, 31
	s_lshl_b64 s[2:3], s[2:3], 21
	s_lshl_b32 s42, s4, 1
	s_add_i32 s10, s10, s11
	s_waitcnt vmcnt(1)
	ds_write_b128 v6, v[104:107]
	s_waitcnt lgkmcnt(0)
	s_barrier
	ds_read_u16 v7, v3
	ds_read_u16 v8, v3 offset:144
	ds_read_u16 v9, v3 offset:288
	ds_read_u16 v12, v3 offset:432
	ds_read_u16 v10, v3 offset:576
	ds_read_u16 v13, v3 offset:720
	ds_read_u16 v11, v3 offset:864
	ds_read_u16 v14, v3 offset:1008
	s_waitcnt lgkmcnt(4)
	v_perm_b32 v9, v12, v9, s6
	v_perm_b32 v8, v8, v7, s6
	s_waitcnt lgkmcnt(2)
	v_perm_b32 v10, v13, v10, s6
	v_lshl_add_u64 v[12:13], v[4:5], 0, s[2:3]
	v_lshl_add_u64 v[12:13], v[12:13], 0, s[42:43]
	s_waitcnt lgkmcnt(0)
	v_perm_b32 v11, v14, v11, s6
	v_lshl_add_u64 v[12:13], v[12:13], 0, v[0:1]
	global_store_dwordx4 v[12:13], v[8:11], off
	s_barrier
	s_cmpk_lt_i32 s10, 0x600
	s_cbranch_scc0 .LBB0_503
	s_bfe_u32 s1, s10, 0x10008
	s_lshl_b32 s4, s10, 6
	s_and_b32 s4, s4, 0x3fc0
	s_ashr_i32 s2, s10, 31
	s_lshr_b32 s2, s2, 23
	s_add_i32 s2, s10, s2
	s_ashr_i32 s2, s2, 9
	s_lshl_b32 s2, s2, 1
	s_or_b32 s2, s2, s1
	s_ashr_i32 s3, s2, 31
	s_lshl_b64 s[2:3], s[2:3], 21
	s_lshl_b32 s42, s4, 1
	s_add_i32 s10, s10, s11
	s_waitcnt vmcnt(0)
	ds_write_b128 v6, v[108:111]
	s_waitcnt lgkmcnt(0)
	s_barrier
	ds_read_u16 v7, v3
	ds_read_u16 v8, v3 offset:144
	ds_read_u16 v9, v3 offset:288
	ds_read_u16 v12, v3 offset:432
	ds_read_u16 v10, v3 offset:576
	ds_read_u16 v13, v3 offset:720
	ds_read_u16 v11, v3 offset:864
	ds_read_u16 v14, v3 offset:1008
	s_waitcnt lgkmcnt(4)
	v_perm_b32 v9, v12, v9, s6
	v_perm_b32 v8, v8, v7, s6
	s_waitcnt lgkmcnt(2)
	v_perm_b32 v10, v13, v10, s6
	v_lshl_add_u64 v[12:13], v[4:5], 0, s[2:3]
	v_lshl_add_u64 v[12:13], v[12:13], 0, s[42:43]
	s_waitcnt lgkmcnt(0)
	v_perm_b32 v11, v14, v11, s6
	v_lshl_add_u64 v[12:13], v[12:13], 0, v[0:1]
	global_store_dwordx4 v[12:13], v[8:11], off
	s_barrier
	s_lshl_b32 s0, s10, 6
	s_cmpk_lt_i32 s10, 0x600
	s_cbranch_scc0 .LBB0_503
